# baseline (speedup 1.0000x reference)
_Z6k_poolPKDF16_PKiS2_PKfS4_S4_Pf:
	s_load_dwordx8 s[4:11], s[0:1], 0x0
	s_load_dwordx4 s[20:23], s[0:1], 0x28
	v_mov_b32_e32 v61, 0
	s_ashr_i32 s3, s2, 31
	s_lshl_b64 s[12:13], s[2:3], 2
	v_lshrrev_b32_e32 v37, 4, v0
	v_bfe_u32 v1, v0, 3, 1
	s_waitcnt lgkmcnt(0)
	s_add_u32 s6, s6, s12
	s_addc_u32 s7, s7, s13
	s_lshl_b32 s12, s2, 9
	s_ashr_i32 s13, s12, 31
	s_lshl_b64 s[12:13], s[12:13], 2
	s_add_u32 s8, s8, s12
	v_add_u32_e32 v1, v1, v37
	s_addc_u32 s9, s9, s13
	v_lshlrev_b32_e32 v3, 2, v1
	global_load_dword v2, v3, s[8:9]
	global_load_dword v4, v3, s[8:9] offset:256
	global_load_dword v10, v3, s[8:9] offset:512
	global_load_dword v14, v3, s[8:9] offset:768
	global_load_dword v18, v3, s[8:9] offset:1024
	global_load_dword v24, v3, s[8:9] offset:1280
	v_min_u32_e32 v1, 63, v1
	v_lshlrev_b32_e32 v1, 2, v1
	global_load_dword v6, v3, s[8:9] offset:1536
	global_load_dword v8, v1, s[8:9] offset:1792
	v_and_b32_e32 v36, 15, v0
	v_mov_b32_e32 v13, 0
	v_lshlrev_b32_e32 v12, 4, v36
	v_lshl_add_u64 v[22:23], s[4:5], 0, v[12:13]
	v_mbcnt_lo_u32_b32 v1, -1, 0
	s_load_dwordx2 s[4:5], s[0:1], 0x20
	v_mbcnt_hi_u32_b32 v1, -1, v1
	v_and_b32_e32 v38, 63, v0
	v_and_b32_e32 v9, 56, v1
	v_lshlrev_b32_e32 v7, 2, v38
	v_cmp_eq_u32_e32 vcc, 56, v9
	s_load_dword s6, s[6:7], 0x0
	v_mov_b32_e32 v40, 0xfc00fc00
	v_cndmask_b32_e64 v9, 8, 0, vcc
	v_add_lshl_u32 v49, v9, v1, 2
	v_or_b32_e32 v41, 64, v37
	v_or_b32_e32 v46, 0x80, v37
	s_mov_b32 s3, 0xfc00
	v_or_b32_e32 v47, 0xc0, v37
	v_or_b32_e32 v48, 0x100, v37
	s_waitcnt vmcnt(7)
	v_ashrrev_i32_e32 v3, 31, v2
	v_lshlrev_b64 v[2:3], 8, v[2:3]
	v_lshl_add_u64 v[2:3], v[22:23], 0, v[2:3]
	s_waitcnt vmcnt(6)
	v_ashrrev_i32_e32 v5, 31, v4
	global_load_dwordx4 v[30:33], v[2:3], off nt
	v_lshlrev_b64 v[2:3], 8, v[4:5]
	v_lshl_add_u64 v[2:3], v[22:23], 0, v[2:3]
	s_waitcnt vmcnt(6)
	v_ashrrev_i32_e32 v11, 31, v10
	global_load_dwordx4 v[26:29], v[2:3], off nt
	v_lshlrev_b64 v[2:3], 8, v[10:11]
	v_lshl_add_u64 v[2:3], v[22:23], 0, v[2:3]
	s_waitcnt vmcnt(6)
	v_ashrrev_i32_e32 v15, 31, v14
	global_load_dwordx4 v[10:13], v[2:3], off nt
	v_lshlrev_b64 v[2:3], 8, v[14:15]
	v_lshl_add_u64 v[2:3], v[22:23], 0, v[2:3]
	s_waitcnt vmcnt(6)
	v_ashrrev_i32_e32 v19, 31, v18
	global_load_dwordx4 v[14:17], v[2:3], off nt
	v_lshlrev_b64 v[2:3], 8, v[18:19]
	v_lshl_add_u64 v[2:3], v[22:23], 0, v[2:3]
	s_waitcnt vmcnt(6)
	v_ashrrev_i32_e32 v25, 31, v24
	global_load_dwordx4 v[18:21], v[2:3], off nt
	v_lshlrev_b64 v[2:3], 8, v[24:25]
	v_lshl_add_u64 v[2:3], v[22:23], 0, v[2:3]
	global_load_dwordx4 v[2:5], v[2:3], off nt
	s_nop 0
	global_load_dword v39, v7, s[10:11]
	s_waitcnt lgkmcnt(0)
	global_load_dword v34, v7, s[4:5]
	global_load_dword v35, v7, s[4:5] offset:256
	s_waitcnt vmcnt(10)
	v_ashrrev_i32_e32 v7, 31, v6
	s_waitcnt vmcnt(9)
	v_ashrrev_i32_e32 v9, 31, v8
	v_lshlrev_b64 v[6:7], 8, v[6:7]
	v_lshlrev_b64 v[8:9], 8, v[8:9]
	v_lshl_add_u64 v[42:43], v[22:23], 0, v[6:7]
	v_lshl_add_u64 v[44:45], v[22:23], 0, v[8:9]
	global_load_dwordx4 v[22:25], v[42:43], off nt
	global_load_dwordx4 v[6:9], v[44:45], off nt
	global_load_dwordx2 v[62:63], v61, s[20:21]
	s_min_i32 s4, s6, 0x1ff
	v_cmp_gt_i32_e32 vcc, s4, v37
	s_waitcnt vmcnt(10)
	ds_bpermute_b32 v42, v49, v30
	ds_bpermute_b32 v43, v49, v31
	ds_bpermute_b32 v44, v49, v32
	ds_bpermute_b32 v45, v49, v33
	s_waitcnt vmcnt(9)
	ds_bpermute_b32 v50, v49, v26
	ds_bpermute_b32 v51, v49, v27
	ds_bpermute_b32 v52, v49, v28
	ds_bpermute_b32 v53, v49, v29
	s_waitcnt vmcnt(8)
	ds_bpermute_b32 v54, v49, v10
	ds_bpermute_b32 v55, v49, v11
	ds_bpermute_b32 v56, v49, v12
	ds_bpermute_b32 v57, v49, v13
	s_waitcnt vmcnt(7)
	ds_bpermute_b32 v58, v49, v14
	ds_bpermute_b32 v59, v49, v15
	s_waitcnt lgkmcnt(13)
	v_pk_add_f16 v30, v30, v42
	s_waitcnt lgkmcnt(12)
	v_pk_add_f16 v31, v31, v43
	s_waitcnt lgkmcnt(11)
	v_pk_add_f16 v32, v32, v44
	s_waitcnt lgkmcnt(10)
	v_pk_add_f16 v33, v33, v45
	ds_bpermute_b32 v42, v49, v16
	ds_bpermute_b32 v43, v49, v17
	s_waitcnt vmcnt(6)
	ds_bpermute_b32 v44, v49, v18
	ds_bpermute_b32 v45, v49, v19
	s_waitcnt lgkmcnt(13)
	v_pk_add_f16 v26, v26, v50
	s_waitcnt lgkmcnt(12)
	v_pk_add_f16 v27, v27, v51
	s_waitcnt lgkmcnt(11)
	v_pk_add_f16 v28, v28, v52
	s_waitcnt lgkmcnt(10)
	v_pk_add_f16 v29, v29, v53
	ds_bpermute_b32 v50, v49, v20
	ds_bpermute_b32 v51, v49, v21
	v_cndmask_b32_e32 v30, v40, v30, vcc
	v_cndmask_b32_e32 v31, v40, v31, vcc
	v_cndmask_b32_e32 v32, v40, v32, vcc
	v_cndmask_b32_e32 v33, v40, v33, vcc
	v_cmp_gt_i32_e32 vcc, s4, v41
	s_waitcnt vmcnt(5)
	ds_bpermute_b32 v52, v49, v2
	s_waitcnt lgkmcnt(12)
	v_pk_add_f16 v10, v10, v54
	s_waitcnt lgkmcnt(11)
	v_pk_add_f16 v11, v11, v55
	s_waitcnt lgkmcnt(10)
	v_pk_add_f16 v12, v12, v56
	s_waitcnt lgkmcnt(9)
	v_pk_add_f16 v13, v13, v57
	v_cndmask_b32_e32 v26, v40, v26, vcc
	v_cndmask_b32_e32 v27, v40, v27, vcc
	v_cndmask_b32_e32 v28, v40, v28, vcc
	v_cndmask_b32_e32 v29, v40, v29, vcc
	v_cmp_gt_i32_e32 vcc, s4, v46
	v_pk_max_f16 v30, v30, v30
	v_pk_max_f16 v31, v31, v31
	s_waitcnt lgkmcnt(8)
	v_pk_add_f16 v14, v14, v58
	s_waitcnt lgkmcnt(7)
	v_pk_add_f16 v15, v15, v59
	v_cndmask_b32_e32 v10, v40, v10, vcc
	v_cndmask_b32_e32 v11, v40, v11, vcc
	v_cndmask_b32_e32 v12, v40, v12, vcc
	v_cndmask_b32_e32 v13, v40, v13, vcc
	v_cmp_gt_i32_e32 vcc, s4, v47
	v_pk_max_f16 v26, v26, v26
	v_pk_max_f16 v27, v27, v27
	v_pk_max_f16 v30, v30, s3 op_sel_hi:[1,0]
	v_pk_max_f16 v31, v31, s3 op_sel_hi:[1,0]
	v_cndmask_b32_e32 v14, v40, v14, vcc
	v_cndmask_b32_e32 v15, v40, v15, vcc
	v_pk_max_f16 v10, v10, v10
	v_pk_max_f16 v11, v11, v11
	v_pk_max_f16 v26, v30, v26
	v_pk_max_f16 v27, v31, v27
	s_waitcnt lgkmcnt(6)
	v_pk_add_f16 v16, v16, v42
	s_waitcnt lgkmcnt(5)
	v_pk_add_f16 v17, v17, v43
	v_pk_max_f16 v14, v14, v14
	v_pk_max_f16 v15, v15, v15
	v_pk_max_f16 v10, v26, v10
	v_pk_max_f16 v11, v27, v11
	s_waitcnt lgkmcnt(4)
	v_pk_add_f16 v18, v18, v44
	s_waitcnt lgkmcnt(3)
	v_pk_add_f16 v19, v19, v45
	s_waitcnt lgkmcnt(2)
	v_pk_add_f16 v20, v20, v50
	s_waitcnt lgkmcnt(1)
	v_pk_add_f16 v21, v21, v51
	v_cndmask_b32_e32 v16, v40, v16, vcc
	v_cndmask_b32_e32 v17, v40, v17, vcc
	v_cmp_gt_i32_e32 vcc, s4, v48
	v_pk_max_f16 v10, v10, v14
	v_pk_max_f16 v11, v11, v15
	v_or_b32_e32 v14, 0x140, v37
	ds_bpermute_b32 v15, v49, v3
	v_cndmask_b32_e32 v18, v40, v18, vcc
	v_cndmask_b32_e32 v19, v40, v19, vcc
	v_cndmask_b32_e32 v20, v40, v20, vcc
	v_cndmask_b32_e32 v21, v40, v21, vcc
	s_waitcnt lgkmcnt(1)
	v_pk_add_f16 v2, v2, v52
	v_cmp_gt_i32_e32 vcc, s4, v14
	v_pk_max_f16 v18, v18, v18
	s_waitcnt lgkmcnt(0)
	v_pk_add_f16 v3, v3, v15
	v_cndmask_b32_e32 v2, v40, v2, vcc
	v_pk_max_f16 v10, v10, v18
	v_pk_max_f16 v2, v2, v2
	v_pk_max_f16 v32, v32, v32
	v_pk_max_f16 v2, v10, v2
	ds_bpermute_b32 v10, v49, v4
	v_pk_max_f16 v19, v19, v19
	v_cndmask_b32_e32 v3, v40, v3, vcc
	v_pk_max_f16 v28, v28, v28
	v_pk_max_f16 v32, v32, s3 op_sel_hi:[1,0]
	v_pk_max_f16 v11, v11, v19
	v_pk_max_f16 v3, v3, v3
	v_pk_max_f16 v12, v12, v12
	v_pk_max_f16 v28, v32, v28
	v_pk_max_f16 v3, v11, v3
	ds_bpermute_b32 v11, v49, v5
	v_pk_max_f16 v16, v16, v16
	v_pk_max_f16 v12, v28, v12
	s_waitcnt lgkmcnt(1)
	v_pk_add_f16 v4, v4, v10
	s_waitcnt vmcnt(2)
	ds_bpermute_b32 v10, v49, v22
	v_pk_max_f16 v20, v20, v20
	v_pk_max_f16 v12, v12, v16
	v_cndmask_b32_e32 v4, v40, v4, vcc
	v_pk_max_f16 v12, v12, v20
	v_pk_max_f16 v4, v4, v4
	s_waitcnt lgkmcnt(1)
	v_pk_add_f16 v5, v5, v11
	v_pk_max_f16 v4, v12, v4
	ds_bpermute_b32 v12, v49, v23
	v_or_b32_e32 v11, 0x180, v37
	v_cndmask_b32_e32 v5, v40, v5, vcc
	s_waitcnt lgkmcnt(1)
	v_pk_add_f16 v10, v22, v10
	v_cmp_gt_i32_e32 vcc, s4, v11
	ds_bpermute_b32 v11, v49, v24
	v_pk_max_f16 v33, v33, v33
	v_cndmask_b32_e32 v10, v40, v10, vcc
	v_pk_max_f16 v10, v10, v10
	v_pk_max_f16 v29, v29, v29
	v_pk_max_f16 v2, v2, v10
	s_waitcnt lgkmcnt(1)
	v_pk_add_f16 v10, v23, v12
	s_waitcnt lgkmcnt(0)
	v_pk_add_f16 v11, v24, v11
	v_cndmask_b32_e32 v10, v40, v10, vcc
	v_pk_max_f16 v10, v10, v10
	v_cndmask_b32_e32 v11, v40, v11, vcc
	v_pk_max_f16 v3, v3, v10
	ds_bpermute_b32 v10, v49, v25
	v_pk_max_f16 v11, v11, v11
	v_pk_max_f16 v33, v33, s3 op_sel_hi:[1,0]
	v_pk_max_f16 v4, v4, v11
	s_waitcnt vmcnt(1)
	ds_bpermute_b32 v11, v49, v6
	v_pk_max_f16 v13, v13, v13
	v_pk_max_f16 v29, v33, v29
	v_pk_max_f16 v17, v17, v17
	v_pk_max_f16 v13, v29, v13
	v_pk_max_f16 v21, v21, v21
	v_pk_max_f16 v13, v13, v17
	s_waitcnt lgkmcnt(1)
	v_pk_add_f16 v10, v25, v10
	v_pk_max_f16 v13, v13, v21
	v_pk_max_f16 v5, v5, v5
	v_cndmask_b32_e32 v10, v40, v10, vcc
	v_pk_max_f16 v5, v13, v5
	v_pk_max_f16 v10, v10, v10
	s_waitcnt lgkmcnt(0)
	v_pk_add_f16 v6, v6, v11
	ds_bpermute_b32 v11, v49, v7
	v_pk_max_f16 v5, v5, v10
	v_or_b32_e32 v10, 0x1c0, v37
	v_cmp_gt_i32_e32 vcc, s4, v10
	s_nop 1
	v_cndmask_b32_e32 v6, v40, v6, vcc
	v_pk_max_f16 v6, v6, v6
	s_nop 0
	v_pk_max_f16 v2, v2, v6
	s_waitcnt lgkmcnt(0)
	v_pk_add_f16 v6, v7, v11
	ds_bpermute_b32 v7, v49, v8
	v_cndmask_b32_e32 v6, v40, v6, vcc
	v_pk_max_f16 v6, v6, v6
	s_waitcnt lgkmcnt(0)
	v_pk_add_f16 v7, v8, v7
	v_pk_max_f16 v6, v3, v6
	ds_bpermute_b32 v3, v49, v9
	v_cndmask_b32_e32 v7, v40, v7, vcc
	v_pk_max_f16 v7, v7, v7
	s_waitcnt lgkmcnt(0)
	v_pk_add_f16 v3, v9, v3
	s_nop 0
	v_cndmask_b32_e32 v3, v40, v3, vcc
	v_pk_max_f16 v7, v4, v7
	v_pk_max_f16 v3, v3, v3
	v_and_b32_e32 v4, 64, v1
	v_pk_max_f16 v9, v5, v3
	v_xor_b32_e32 v3, 16, v1
	v_add_u32_e32 v4, 64, v4
	v_cmp_lt_i32_e32 vcc, v3, v4
	s_nop 1
	v_cndmask_b32_e32 v3, v1, v3, vcc
	v_lshlrev_b32_e32 v8, 2, v3
	ds_bpermute_b32 v5, v8, v2
	v_xor_b32_e32 v3, 32, v1
	ds_bpermute_b32 v11, v8, v6
	v_cmp_lt_i32_e32 vcc, v3, v4
	s_nop 1
	v_cndmask_b32_e32 v3, v1, v3, vcc
	v_lshlrev_b32_e32 v10, 2, v3
	s_waitcnt lgkmcnt(1)
	v_pk_max_f16 v3, v5, v5
	s_waitcnt lgkmcnt(0)
	v_pk_max_f16 v5, v11, v11
	v_pk_max_f16 v3, v2, v3
	ds_bpermute_b32 v2, v8, v7
	ds_bpermute_b32 v11, v8, v9
	v_pk_max_f16 v5, v6, v5
	ds_bpermute_b32 v4, v10, v3
	ds_bpermute_b32 v6, v10, v5
	s_waitcnt lgkmcnt(3)
	v_pk_max_f16 v2, v2, v2
	v_cmp_gt_u32_e32 vcc, 8, v38
	v_pk_max_f16 v7, v7, v2
	s_waitcnt lgkmcnt(2)
	v_pk_max_f16 v2, v11, v11
	ds_bpermute_b32 v8, v10, v7
	v_pk_max_f16 v9, v9, v2
	ds_bpermute_b32 v10, v10, v9
	v_lshlrev_b32_e32 v2, 2, v0
	s_and_saveexec_b64 s[4:5], vcc
	s_cbranch_execz .LBB2_2
	s_waitcnt lgkmcnt(0)
	v_pk_max_f16 v10, v10, v10
	v_pk_max_f16 v9, v9, v9
	v_pk_max_f16 v8, v8, v8
	v_pk_max_f16 v7, v7, v7
	v_pk_max_f16 v6, v6, v6
	v_pk_max_f16 v5, v5, v5
	v_pk_max_f16 v4, v4, v4
	v_pk_max_f16 v3, v3, v3
	v_pk_max_f16 v11, v9, v10
	v_pk_max_f16 v9, v7, v8
	v_pk_max_f16 v7, v5, v6
	v_pk_max_f16 v3, v3, v4
	v_cvt_f32_f16_e32 v6, v7
	v_cvt_f32_f16_e32 v4, v3
	v_cvt_f32_f16_sdwa v5, v3 dst_sel:DWORD dst_unused:UNUSED_PAD src0_sel:WORD_1
	v_cvt_f32_f16_sdwa v7, v7 dst_sel:DWORD dst_unused:UNUSED_PAD src0_sel:WORD_1
	v_cvt_f32_f16_e32 v8, v9
	v_cvt_f32_f16_sdwa v9, v9 dst_sel:DWORD dst_unused:UNUSED_PAD src0_sel:WORD_1
	v_cvt_f32_f16_e32 v10, v11
	v_cvt_f32_f16_sdwa v11, v11 dst_sel:DWORD dst_unused:UNUSED_PAD src0_sel:WORD_1
	v_and_b32_e32 v3, 0xf00, v2
	v_lshl_add_u32 v3, v36, 5, v3
	ds_write_b128 v3, v[4:7]
	ds_write_b128 v3, v[8:11] offset:16
.LBB2_2:
	s_or_b64 exec, exec, s[4:5]
	v_cmp_gt_u32_e32 vcc, 64, v0
	s_waitcnt lgkmcnt(0)
	s_barrier
	s_and_saveexec_b64 s[4:5], vcc
	s_cbranch_execz .LBB2_5
	ds_read2st64_b32 v[4:5], v2 offset1:1
	ds_read2st64_b32 v[6:7], v2 offset0:2 offset1:3
	ds_read2st64_b32 v[8:9], v2 offset0:4 offset1:5
	ds_read2st64_b32 v[10:11], v2 offset0:6 offset1:7
	s_waitcnt lgkmcnt(3)
	v_max_f32_e32 v3, v5, v5
	v_max_f32_e32 v4, v4, v4
	v_max_f32_e32 v3, v4, v3
	s_waitcnt lgkmcnt(2)
	v_max3_f32 v3, v3, v6, v7
	s_waitcnt lgkmcnt(1)
	v_max3_f32 v12, v3, v8, v9
	ds_read2st64_b32 v[4:5], v2 offset0:8 offset1:9
	ds_read2st64_b32 v[6:7], v2 offset0:10 offset1:11
	ds_read2st64_b32 v[8:9], v2 offset0:12 offset1:13
	ds_read2st64_b32 v[2:3], v2 offset0:14 offset1:15
	s_waitcnt lgkmcnt(4)
	v_max3_f32 v10, v12, v10, v11
	s_waitcnt lgkmcnt(3)
	v_max3_f32 v4, v10, v4, v5
	s_waitcnt lgkmcnt(2)
	v_max3_f32 v4, v4, v6, v7
	s_waitcnt lgkmcnt(1)
	v_max3_f32 v4, v4, v8, v9
	s_waitcnt lgkmcnt(0)
	v_max3_f32 v2, v4, v2, v3
	v_add_f32_e32 v2, v39, v2
	v_mul_f32_e32 v4, v34, v2
	v_mul_f32_e32 v5, v35, v2
	s_nop 1
	v_add_f32_dpp v4, v4, v4 quad_perm:[1,0,3,2] row_mask:0xf bank_mask:0xf
	v_add_f32_dpp v5, v5, v5 quad_perm:[1,0,3,2] row_mask:0xf bank_mask:0xf
	s_nop 1
	v_add_f32_dpp v4, v4, v4 quad_perm:[2,3,0,1] row_mask:0xf bank_mask:0xf
	v_add_f32_dpp v5, v5, v5 quad_perm:[2,3,0,1] row_mask:0xf bank_mask:0xf
	s_nop 1
	v_add_f32_dpp v4, v4, v4 row_half_mirror row_mask:0xf bank_mask:0xf
	v_add_f32_dpp v5, v5, v5 row_half_mirror row_mask:0xf bank_mask:0xf
	s_nop 1
	v_add_f32_dpp v4, v4, v4 row_mirror row_mask:0xf bank_mask:0xf
	v_add_f32_dpp v5, v5, v5 row_mirror row_mask:0xf bank_mask:0xf
	s_nop 1
	v_readlane_b32 s4, v4, 16
	v_readlane_b32 s5, v4, 32
	v_readlane_b32 s6, v4, 48
	v_readlane_b32 s7, v5, 16
	v_readlane_b32 s12, v5, 32
	v_readlane_b32 s13, v5, 48
	s_lshl_b32 s0, s2, 1
	s_ashr_i32 s1, s0, 31
	s_lshl_b64 s[0:1], s[0:1], 2
	v_add_f32_e32 v4, s4, v4
	v_add_f32_e32 v5, s7, v5
	v_add_f32_e32 v4, s5, v4
	v_add_f32_e32 v5, s12, v5
	v_add_f32_e32 v4, s6, v4
	v_add_f32_e32 v5, s13, v5
	s_add_u32 s0, s22, s0
	s_addc_u32 s1, s23, s1
	v_cmp_eq_u32_e32 vcc, 0, v0
	s_and_b64 exec, exec, vcc
	s_cbranch_execz .LBB2_5
	v_mov_b32_e32 v6, 0
	s_waitcnt vmcnt(0)
	v_add_f32_e32 v0, v62, v4
	v_add_f32_e32 v1, v63, v5
	global_store_dwordx2 v6, v[0:1], s[0:1]

	.amdhsa_kernel _Z6k_poolPKDF16_PKiS2_PKfS4_S4_Pf
		.amdhsa_group_segment_fixed_size 4096
		.amdhsa_private_segment_fixed_size 0
		.amdhsa_kernarg_size 56
		.amdhsa_user_sgpr_count 2
		.amdhsa_user_sgpr_dispatch_ptr 0
		.amdhsa_user_sgpr_queue_ptr 0
		.amdhsa_user_sgpr_kernarg_segment_ptr 1
		.amdhsa_user_sgpr_dispatch_id 0
		.amdhsa_user_sgpr_kernarg_preload_length 0
		.amdhsa_user_sgpr_kernarg_preload_offset 0
		.amdhsa_user_sgpr_private_segment_size 0
		.amdhsa_uses_dynamic_stack 0
		.amdhsa_enable_private_segment 0
		.amdhsa_system_sgpr_workgroup_id_x 1
		.amdhsa_system_sgpr_workgroup_id_y 0
		.amdhsa_system_sgpr_workgroup_id_z 0
		.amdhsa_system_sgpr_workgroup_info 0
		.amdhsa_system_vgpr_workitem_id 0
		.amdhsa_next_free_vgpr 64
		.amdhsa_next_free_sgpr 24
		.amdhsa_accum_offset 64
		.amdhsa_reserve_vcc 1
		.amdhsa_float_round_mode_32 0
		.amdhsa_float_round_mode_16_64 0
		.amdhsa_float_denorm_mode_32 3
		.amdhsa_float_denorm_mode_16_64 3
		.amdhsa_dx10_clamp 1
		.amdhsa_ieee_mode 1
		.amdhsa_fp16_overflow 0
		.amdhsa_tg_split 0
		.amdhsa_exception_fp_ieee_invalid_op 0
		.amdhsa_exception_fp_denorm_src 0
		.amdhsa_exception_fp_ieee_div_zero 0
		.amdhsa_exception_fp_ieee_overflow 0
		.amdhsa_exception_fp_ieee_underflow 0
		.amdhsa_exception_fp_ieee_inexact 0
		.amdhsa_exception_int_div_zero 0
	.end_amdhsa_kernel

amdhsa.kernels:
  - .agpr_count:     0
    .args:
      - .actual_access:  read_only
        .address_space:  global
        .offset:         0
        .size:           8
        .value_kind:     global_buffer
      - .actual_access:  read_only
        .address_space:  global
        .offset:         8
        .size:           8
        .value_kind:     global_buffer
      - .actual_access:  write_only
        .address_space:  global
        .offset:         16
        .size:           8
        .value_kind:     global_buffer
      - .actual_access:  write_only
        .address_space:  global
        .offset:         24
        .size:           8
        .value_kind:     global_buffer
      - .actual_access:  write_only
        .address_space:  global
        .offset:         32
        .size:           8
        .value_kind:     global_buffer
      - .actual_access:  write_only
        .address_space:  global
        .offset:         40
        .size:           8
        .value_kind:     global_buffer
    .group_segment_fixed_size: 32
    .kernarg_segment_align: 8
    .kernarg_segment_size: 48
    .language:       OpenCL C
    .language_version:
      - 2
      - 0
    .max_flat_workgroup_size: 512
    .name:           _Z6k_prepPKiPKfPiS3_P15HIP_vector_typeIjLj4EEPh
    .private_segment_fixed_size: 0
    .sgpr_count:     16
    .sgpr_spill_count: 0
    .symbol:         _Z6k_prepPKiPKfPiS3_P15HIP_vector_typeIjLj4EEPh.kd
    .uniform_work_group_size: 1
    .uses_dynamic_stack: false
    .vgpr_count:     36
    .vgpr_spill_count: 0
    .wavefront_size: 64
  - .agpr_count:     0
    .args:
      - .actual_access:  read_only
        .address_space:  global
        .offset:         0
        .size:           8
        .value_kind:     global_buffer
      - .actual_access:  read_only
        .address_space:  global
        .offset:         8
        .size:           8
        .value_kind:     global_buffer
      - .actual_access:  read_only
        .address_space:  global
        .offset:         16
        .size:           8
        .value_kind:     global_buffer
      - .actual_access:  write_only
        .address_space:  global
        .offset:         24
        .size:           8
        .value_kind:     global_buffer
      - .actual_access:  read_only
        .address_space:  global
        .offset:         32
        .size:           8
        .value_kind:     global_buffer
    .group_segment_fixed_size: 0
    .kernarg_segment_align: 8
    .kernarg_segment_size: 40
    .language:       OpenCL C
    .language_version:
      - 2
      - 0
    .max_flat_workgroup_size: 256
    .name:           _Z6k_gemmPKfS0_PK15HIP_vector_typeIjLj4EEPDF16_PKh
    .private_segment_fixed_size: 0
    .sgpr_count:     48
    .sgpr_spill_count: 0
    .symbol:         _Z6k_gemmPKfS0_PK15HIP_vector_typeIjLj4EEPDF16_PKh.kd
    .uniform_work_group_size: 1
    .uses_dynamic_stack: false
    .vgpr_count:     230
    .vgpr_spill_count: 0
    .wavefront_size: 64
  - .agpr_count:     0
    .args:
      - .actual_access:  read_only
        .address_space:  global
        .offset:         0
        .size:           8
        .value_kind:     global_buffer
      - .actual_access:  read_only
        .address_space:  global
        .offset:         8
        .size:           8
        .value_kind:     global_buffer
      - .actual_access:  read_only
        .address_space:  global
        .offset:         16
        .size:           8
        .value_kind:     global_buffer
      - .actual_access:  read_only
        .address_space:  global
        .offset:         24
        .size:           8
        .value_kind:     global_buffer
      - .actual_access:  read_only
        .address_space:  global
        .offset:         32
        .size:           8
        .value_kind:     global_buffer
      - .actual_access:  read_only
        .address_space:  global
        .offset:         40
        .size:           8
        .value_kind:     global_buffer
      - .actual_access:  write_only
        .address_space:  global
        .offset:         48
        .size:           8
        .value_kind:     global_buffer
    .group_segment_fixed_size: 4096
    .kernarg_segment_align: 8
    .kernarg_segment_size: 56
    .language:       OpenCL C
    .language_version:
      - 2
      - 0
    .max_flat_workgroup_size: 1024
    .name:           _Z6k_poolPKDF16_PKiS2_PKfS4_S4_Pf
    .private_segment_fixed_size: 0
    .sgpr_count:     30
    .sgpr_spill_count: 0
    .symbol:         _Z6k_poolPKDF16_PKiS2_PKfS4_S4_Pf.kd
    .uniform_work_group_size: 1
    .uses_dynamic_stack: false
    .vgpr_count:     64
    .vgpr_spill_count: 0
    .wavefront_size: 64
